# expert-weight f32->bf16 conversion without the LDS transpose: each lane loads an 8k x 4n f32 block and stores four bf16x8 chunks directly (same RNE v_cvt_pk_bf16_f32), 4-deep counted-vmcnt pipeline, t
# speedup vs baseline: 1.0088x; 1.0088x over previous
; __device__ __forceinline__ void t_load(const TItem& d, f32x4 (&r)[8], int lane) {
; __global__ void __launch_bounds__(512, 2) mk_fwd(Params p_unused) {
;     ...
;         {
;             const int tid = otid(), lane = tid & 63, wave = __builtin_amdgcn_readfirstlane(tid >> 6);
;             LAS float* scr = (LAS float*)(L + wave * 16384);
;             unsigned* qc = WSP(unsigned, WS_CTL) + CW_Q;
;             constexpr int I_G = (DM / 64) * (DE / 32), I_D = (DE / 64) * (DM / 32), PER = 2 * I_G + I_D; constexpr unsigned NTICK = 64u * PER / 2u;
;             auto decode = [&](int it) { TItem d; const int le = it / PER; int r = it - le * PER;
;                 if (r < I_G) { d.W = kp->w_gate + (size_t)le * DM * DE; d.WT = WSP(bf16_t, WS_WGU) + (size_t)le * 2048 * DM; d.K = DM; d.N = DE; d.kind = 1; }
;                 else if ((r -= I_G) < I_G) { d.W = kp->w_up + (size_t)le * DM * DE; d.WT = WSP(bf16_t, WS_WGU) + (size_t)le * 2048 * DM; d.K = DM; d.N = DE; d.kind = 2; }
;                 else { r -= I_G; d.W = kp->w_down + (size_t)le * DE * DM; d.WT = WSP(bf16_t, WS_WD) + (size_t)le * DM * DE; d.K = DE; d.N = DM; d.kind = 0; }
;                 const int nblk = d.N / 32; d.k0 = 64 * (r / nblk); d.n0 = 32 * (r % nblk); return d; };
;             static_assert(NTICK % 8u == 0u, "ticket chunks");
;             auto grab = [&]() { unsigned t = 0; if (lane == 0) t = __hip_atomic_fetch_add(qc, 8u, __ATOMIC_RELAXED, __HIP_MEMORY_SCOPE_AGENT); return (unsigned)__builtin_amdgcn_readfirstlane((int)t); };
;             for (unsigned tb = grab(); tb < NTICK; tb = grab()) {
;                 TItem a0 = decode((int)(2u * tb)); TItem a1 = a0; a1.n0 += 32;
;                 f32x4 ra[8], rb[8], rc[8], rd[8]; t_load(a0, ra, lane); t_load(a1, rb, lane);
;                 _Pragma("unroll 1") for (unsigned u = 0; u < 8u; u += 2u) {
;                     const TItem b0 = decode((int)(2u * (tb + u + 1u))); TItem b1 = b0; b1.n0 += 32;
;                     t_load(b0, rc, lane); t_load(b1, rd, lane);
;                     t_store(a0, ra, scr, lane); t_store(a1, rb, scr, lane);
;                     if (u + 2u < 8u) { a0 = decode((int)(2u * (tb + u + 2u))); a1 = a0; a1.n0 += 32; t_load(a0, ra, lane); t_load(a1, rb, lane); }
;                     t_store(b0, rc, scr, lane); t_store(b1, rd, scr, lane);
;                 }
;             }
;         }
.LBB0_468:
	s_load_dwordx2 s[42:43], s[30:31], 0x80
	s_load_dwordx2 s[44:45], s[30:31], 0x88
	s_load_dwordx2 s[46:47], s[30:31], 0x90
	s_add_u32 s4, s28, 0x3000
	s_addc_u32 s5, s29, 0
	s_add_u32 s36, s28, 0x21800000
	s_addc_u32 s37, s29, 0
	s_add_u32 s38, s28, 0x1800000
	s_addc_u32 s39, s29, 0
	v_and_b32_e32 v1, 63, v0
	v_lshrrev_b32_e32 v2, 3, v1
	v_and_b32_e32 v3, 7, v1
	v_lshlrev_b32_e32 v4, 4, v3
	v_lshlrev_b32_e32 v5, 4, v2
	v_lshl_or_b32 v10, v2, 15, v4
	v_lshl_or_b32 v18, v2, 16, v4
	v_lshl_or_b32 v26, v3, 14, v5
	v_lshl_or_b32 v30, v3, 13, v5
	v_add_u32_e32 v11, 0x1000, v10
	v_add_u32_e32 v19, 0x2000, v18
	v_add_u32_e32 v12, 0x2000, v10
	v_add_u32_e32 v20, 0x4000, v18
	v_add_u32_e32 v13, 0x3000, v10
	v_add_u32_e32 v21, 0x6000, v18
	v_add_u32_e32 v14, 0x4000, v10
	v_add_u32_e32 v22, 0x8000, v18
	v_add_u32_e32 v15, 0x5000, v10
	v_add_u32_e32 v23, 0xa000, v18
	v_add_u32_e32 v16, 0x6000, v10
	v_add_u32_e32 v24, 0xc000, v18
	v_add_u32_e32 v17, 0x7000, v10
	v_add_u32_e32 v25, 0xe000, v18
	v_add_u32_e32 v27, 0x1000, v26
	v_add_u32_e32 v31, 0x800, v30
	v_add_u32_e32 v28, 0x2000, v26
	v_add_u32_e32 v32, 0x1000, v30
	v_add_u32_e32 v29, 0x3000, v26
	v_add_u32_e32 v33, 0x1800, v30
	v_mov_b32_e32 v9, 0
	v_mov_b32_e32 v8, 8
	s_waitcnt lgkmcnt(0)
	s_mov_b64 exec, 1
	global_atomic_add v7, v9, v8, s[4:5] sc0
	s_mov_b64 exec, -1
	s_waitcnt vmcnt(0)
	v_readfirstlane_b32 s40, v7
	s_nop 3
.Lcv_loop:
	s_cmp_gt_u32 s40, 0x17fff
	s_cbranch_scc1 .Lcv_done
	s_mov_b64 exec, 1
	global_atomic_add v7, v9, v8, s[4:5] sc0
	s_mov_b64 exec, -1
	s_mul_hi_u32 s6, s40, 0xaaaaaaab
	s_lshr_b32 s10, s6, 10
	s_mul_i32 s6, s10, 0x600
	s_sub_u32 s11, s40, s6
	s_lshl_b32 s11, s11, 1
	s_lshl_b32 s16, s10, 23
	s_cmp_lt_u32 s11, 0x800
	s_cbranch_scc0 .Lcv_down
	s_cmp_lt_u32 s11, 0x400
	s_cselect_b32 s17, 0, 128
	s_cselect_b32 s8, s42, s44
	s_cselect_b32 s9, s43, s45
	s_and_b32 s11, s11, 0x3ff
	s_lshr_b32 s18, s11, 5
	s_lshl_b32 s18, s18, 6
	s_and_b32 s19, s11, 31
	s_lshl_b32 s19, s19, 5
	s_lshl_b32 s20, s18, 12
	s_lshl_b32 s21, s19, 2
	s_add_u32 s20, s20, s21
	s_add_u32 s20, s20, s16
	s_add_u32 s8, s8, s20
	s_addc_u32 s9, s9, 0
	s_lshl_b32 s21, s18, 1
	s_add_u32 s21, s21, s16
	s_add_u32 s12, s38, s21
	s_addc_u32 s13, s39, 0
	s_lshr_b32 s24, s19, 7
	s_lshl_b32 s24, s24, 8
	s_add_u32 s24, s24, s17
	v_mov_b32_e32 v34, v10
	v_mov_b32_e32 v35, v11
	v_mov_b32_e32 v36, v12
	v_mov_b32_e32 v37, v13
	v_mov_b32_e32 v38, v14
	v_mov_b32_e32 v39, v15
	v_mov_b32_e32 v40, v16
	v_mov_b32_e32 v41, v17
	v_mov_b32_e32 v42, v26
	v_mov_b32_e32 v43, v27
	v_mov_b32_e32 v44, v28
	v_mov_b32_e32 v45, v29
	s_mov_b32 s25, 0
	s_mov_b32 s26, 12
	s_branch .Lcv_go
.Lcv_down:
	s_sub_u32 s11, s11, 0x800
	s_lshr_b32 s18, s11, 6
	s_lshl_b32 s18, s18, 6
	s_and_b32 s19, s11, 63
	s_lshl_b32 s19, s19, 5
	s_lshl_b32 s20, s18, 13
	s_lshl_b32 s21, s19, 2
	s_add_u32 s20, s20, s21
	s_add_u32 s20, s20, s16
	s_add_u32 s8, s46, s20
	s_addc_u32 s9, s47, 0
	s_lshr_b32 s21, s16, 1
	s_lshl_b32 s22, s18, 1
	s_add_u32 s21, s21, s22
	s_add_u32 s12, s36, s21
	s_addc_u32 s13, s37, 0
	s_mov_b32 s24, s19
	v_mov_b32_e32 v34, v18
	v_mov_b32_e32 v35, v19
	v_mov_b32_e32 v36, v20
	v_mov_b32_e32 v37, v21
	v_mov_b32_e32 v38, v22
	v_mov_b32_e32 v39, v23
	v_mov_b32_e32 v40, v24
	v_mov_b32_e32 v41, v25
	v_mov_b32_e32 v42, v30
	v_mov_b32_e32 v43, v31
	v_mov_b32_e32 v44, v32
	v_mov_b32_e32 v45, v33
	s_mov_b32 s25, 1
	s_mov_b32 s26, 11
.Lcv_go:
	global_load_dwordx4 v[54:57], v34, s[8:9] offset:0 nt
	global_load_dwordx4 v[58:61], v35, s[8:9] offset:0 nt
	global_load_dwordx4 v[62:65], v36, s[8:9] offset:0 nt
	global_load_dwordx4 v[66:69], v37, s[8:9] offset:0 nt
	global_load_dwordx4 v[70:73], v38, s[8:9] offset:0 nt
	global_load_dwordx4 v[74:77], v39, s[8:9] offset:0 nt
	global_load_dwordx4 v[78:81], v40, s[8:9] offset:0 nt
	global_load_dwordx4 v[82:85], v41, s[8:9] offset:0 nt
	global_load_dwordx4 v[86:89], v34, s[8:9] offset:128 nt
	global_load_dwordx4 v[90:93], v35, s[8:9] offset:128 nt
	global_load_dwordx4 v[94:97], v36, s[8:9] offset:128 nt
	global_load_dwordx4 v[98:101], v37, s[8:9] offset:128 nt
	global_load_dwordx4 v[102:105], v38, s[8:9] offset:128 nt
	global_load_dwordx4 v[106:109], v39, s[8:9] offset:128 nt
	global_load_dwordx4 v[110:113], v40, s[8:9] offset:128 nt
	global_load_dwordx4 v[114:117], v41, s[8:9] offset:128 nt
	global_load_dwordx4 v[118:121], v34, s[8:9] offset:256 nt
	global_load_dwordx4 v[122:125], v35, s[8:9] offset:256 nt
	global_load_dwordx4 v[126:129], v36, s[8:9] offset:256 nt
	global_load_dwordx4 v[130:133], v37, s[8:9] offset:256 nt
	global_load_dwordx4 v[134:137], v38, s[8:9] offset:256 nt
	global_load_dwordx4 v[138:141], v39, s[8:9] offset:256 nt
	global_load_dwordx4 v[142:145], v40, s[8:9] offset:256 nt
	global_load_dwordx4 v[146:149], v41, s[8:9] offset:256 nt
	global_load_dwordx4 v[166:169], v34, s[8:9] offset:384 nt
	global_load_dwordx4 v[170:173], v35, s[8:9] offset:384 nt
	global_load_dwordx4 v[174:177], v36, s[8:9] offset:384 nt
	global_load_dwordx4 v[178:181], v37, s[8:9] offset:384 nt
	global_load_dwordx4 v[182:185], v38, s[8:9] offset:384 nt
	global_load_dwordx4 v[186:189], v39, s[8:9] offset:384 nt
	global_load_dwordx4 v[190:193], v40, s[8:9] offset:384 nt
	global_load_dwordx4 v[194:197], v41, s[8:9] offset:384 nt
	s_waitcnt vmcnt(24)
; #define GAS __attribute__((address_space(1)))
; #define LAS __attribute__((address_space(3)))
; #define LDS_WAIT() asm volatile("s_waitcnt lgkmcnt(0)" ::: "memory")
; __device__ __forceinline__ unsigned pk2(float lo, float hi) { unsigned r; asm("v_cvt_pk_bf16_f32 %0, %1, %2" : "=v"(r) : "v"(lo), "v"(hi)); return r; }
; __device__ __forceinline__ void t_store(const TItem& d, const f32x4 (&r)[8], LAS float* scr, int lane) {
; #pragma unroll
;     for (int i = 0; i < 8; ++i) *(LAS f32x4*)(scr + (8 * i + (lane >> 3)) * 32 + (((lane & 7) * 4 + 8 * i) & 31)) = r[i];
;     LDS_WAIT(); asm volatile("" ::: "memory");
;     const int c = lane >> 3, nl = lane & 7;
; #pragma unroll
;     for (int j = 0; j < 4; ++j) { const int n = nl + 8 * j; const LAS float* s = scr + (8 * c) * 32 + ((n + 8 * c) & 31);
;         v4u o; o.x = pk2(s[0 * 32], s[1 * 32]); o.y = pk2(s[2 * 32], s[3 * 32]); o.z = pk2(s[4 * 32], s[5 * 32]); o.w = pk2(s[6 * 32], s[7 * 32]);
;         __builtin_nontemporal_store(o, (GAS v4u*)(d.WT + (size_t)t_drow(d.kind, d.n0 + n) * d.K + d.k0 + 8 * c)); }
; __global__ void __launch_bounds__(512, 2) mk_fwd(Params p_unused) {
;     ...
;             for (unsigned tb = grab(); tb < NTICK; tb = grab()) {
;                 TItem a0 = decode((int)(2u * tb)); TItem a1 = a0; a1.n0 += 32;
;                 f32x4 ra[8], rb[8], rc[8], rd[8]; t_load(a0, ra, lane); t_load(a1, rb, lane);
;                 _Pragma("unroll 1") for (unsigned u = 0; u < 8u; u += 2u) {
;                     const TItem b0 = decode((int)(2u * (tb + u + 1u))); TItem b1 = b0; b1.n0 += 32;
;                     t_load(b0, rc, lane); t_load(b1, rd, lane);
;                     t_store(a0, ra, scr, lane); t_store(a1, rb, scr, lane);
;                     if (u + 2u < 8u) { a0 = decode((int)(2u * (tb + u + 2u))); a1 = a0; a1.n0 += 32; t_load(a0, ra, lane); t_load(a1, rb, lane); }
;                     t_store(b0, rc, scr, lane); t_store(b1, rd, scr, lane);
;                 }
	s_cmp_eq_u32 s25, 0
	s_movk_i32 s6, 0x0
	s_cmovk_i32 s6, 0x0
	s_add_u32 s6, s6, s24
	s_lshl_b32 s6, s6, s26
	s_add_u32 s14, s12, s6
	s_addc_u32 s15, s13, 0
	v_cvt_pk_bf16_f32 v46, v54, v58
	v_cvt_pk_bf16_f32 v47, v62, v66
	v_cvt_pk_bf16_f32 v48, v70, v74
	v_cvt_pk_bf16_f32 v49, v78, v82
	global_store_dwordx4 v42, v[46:49], s[14:15] nt
	v_cvt_pk_bf16_f32 v50, v55, v59
	v_cvt_pk_bf16_f32 v51, v63, v67
	v_cvt_pk_bf16_f32 v52, v71, v75
	v_cvt_pk_bf16_f32 v53, v79, v83
	global_store_dwordx4 v43, v[50:53], s[14:15] nt
	v_cvt_pk_bf16_f32 v46, v56, v60
	v_cvt_pk_bf16_f32 v47, v64, v68
	v_cvt_pk_bf16_f32 v48, v72, v76
	v_cvt_pk_bf16_f32 v49, v80, v84
	global_store_dwordx4 v44, v[46:49], s[14:15] nt
	v_cvt_pk_bf16_f32 v50, v57, v61
	v_cvt_pk_bf16_f32 v51, v65, v69
	v_cvt_pk_bf16_f32 v52, v73, v77
	v_cvt_pk_bf16_f32 v53, v81, v85
	global_store_dwordx4 v45, v[50:53], s[14:15] nt
	global_load_dwordx4 v[54:57], v34, s[8:9] offset:512 nt
	global_load_dwordx4 v[58:61], v35, s[8:9] offset:512 nt
	global_load_dwordx4 v[62:65], v36, s[8:9] offset:512 nt
	global_load_dwordx4 v[66:69], v37, s[8:9] offset:512 nt
	global_load_dwordx4 v[70:73], v38, s[8:9] offset:512 nt
	global_load_dwordx4 v[74:77], v39, s[8:9] offset:512 nt
	global_load_dwordx4 v[78:81], v40, s[8:9] offset:512 nt
	global_load_dwordx4 v[82:85], v41, s[8:9] offset:512 nt
	s_waitcnt vmcnt(28)
	s_cmp_eq_u32 s25, 0
	s_movk_i32 s6, 0x20
	s_cmovk_i32 s6, 0x20
	s_add_u32 s6, s6, s24
	s_lshl_b32 s6, s6, s26
	s_add_u32 s14, s12, s6
	s_addc_u32 s15, s13, 0
	v_cvt_pk_bf16_f32 v46, v86, v90
	v_cvt_pk_bf16_f32 v47, v94, v98
	v_cvt_pk_bf16_f32 v48, v102, v106
	v_cvt_pk_bf16_f32 v49, v110, v114
	global_store_dwordx4 v42, v[46:49], s[14:15] nt
	v_cvt_pk_bf16_f32 v50, v87, v91
	v_cvt_pk_bf16_f32 v51, v95, v99
	v_cvt_pk_bf16_f32 v52, v103, v107
	v_cvt_pk_bf16_f32 v53, v111, v115
	global_store_dwordx4 v43, v[50:53], s[14:15] nt
	v_cvt_pk_bf16_f32 v46, v88, v92
	v_cvt_pk_bf16_f32 v47, v96, v100
	v_cvt_pk_bf16_f32 v48, v104, v108
	v_cvt_pk_bf16_f32 v49, v112, v116
	global_store_dwordx4 v44, v[46:49], s[14:15] nt
	v_cvt_pk_bf16_f32 v50, v89, v93
	v_cvt_pk_bf16_f32 v51, v97, v101
	v_cvt_pk_bf16_f32 v52, v105, v109
	v_cvt_pk_bf16_f32 v53, v113, v117
	global_store_dwordx4 v45, v[50:53], s[14:15] nt
	global_load_dwordx4 v[86:89], v34, s[8:9] offset:640 nt
	global_load_dwordx4 v[90:93], v35, s[8:9] offset:640 nt
	global_load_dwordx4 v[94:97], v36, s[8:9] offset:640 nt
	global_load_dwordx4 v[98:101], v37, s[8:9] offset:640 nt
	global_load_dwordx4 v[102:105], v38, s[8:9] offset:640 nt
	global_load_dwordx4 v[106:109], v39, s[8:9] offset:640 nt
	global_load_dwordx4 v[110:113], v40, s[8:9] offset:640 nt
	global_load_dwordx4 v[114:117], v41, s[8:9] offset:640 nt
	s_waitcnt vmcnt(32)
	s_cmp_eq_u32 s25, 0
	s_movk_i32 s6, 0x40
	s_cmovk_i32 s6, 0x40
	s_add_u32 s6, s6, s24
	s_lshl_b32 s6, s6, s26
	s_add_u32 s14, s12, s6
	s_addc_u32 s15, s13, 0
	v_cvt_pk_bf16_f32 v46, v118, v122
	v_cvt_pk_bf16_f32 v47, v126, v130
	v_cvt_pk_bf16_f32 v48, v134, v138
	v_cvt_pk_bf16_f32 v49, v142, v146
	global_store_dwordx4 v42, v[46:49], s[14:15] nt
	v_cvt_pk_bf16_f32 v50, v119, v123
	v_cvt_pk_bf16_f32 v51, v127, v131
	v_cvt_pk_bf16_f32 v52, v135, v139
	v_cvt_pk_bf16_f32 v53, v143, v147
	global_store_dwordx4 v43, v[50:53], s[14:15] nt
	v_cvt_pk_bf16_f32 v46, v120, v124
	v_cvt_pk_bf16_f32 v47, v128, v132
	v_cvt_pk_bf16_f32 v48, v136, v140
	v_cvt_pk_bf16_f32 v49, v144, v148
	global_store_dwordx4 v44, v[46:49], s[14:15] nt
	v_cvt_pk_bf16_f32 v50, v121, v125
	v_cvt_pk_bf16_f32 v51, v129, v133
	v_cvt_pk_bf16_f32 v52, v137, v141
	v_cvt_pk_bf16_f32 v53, v145, v149
	global_store_dwordx4 v45, v[50:53], s[14:15] nt
	global_load_dwordx4 v[118:121], v34, s[8:9] offset:768 nt
	global_load_dwordx4 v[122:125], v35, s[8:9] offset:768 nt
	global_load_dwordx4 v[126:129], v36, s[8:9] offset:768 nt
	global_load_dwordx4 v[130:133], v37, s[8:9] offset:768 nt
	global_load_dwordx4 v[134:137], v38, s[8:9] offset:768 nt
	global_load_dwordx4 v[138:141], v39, s[8:9] offset:768 nt
	global_load_dwordx4 v[142:145], v40, s[8:9] offset:768 nt
	global_load_dwordx4 v[146:149], v41, s[8:9] offset:768 nt
	s_waitcnt vmcnt(36)
	s_cmp_eq_u32 s25, 0
	s_movk_i32 s6, 0x60
	s_cmovk_i32 s6, 0x60
	s_add_u32 s6, s6, s24
	s_lshl_b32 s6, s6, s26
	s_add_u32 s14, s12, s6
	s_addc_u32 s15, s13, 0
	v_cvt_pk_bf16_f32 v46, v166, v170
	v_cvt_pk_bf16_f32 v47, v174, v178
	v_cvt_pk_bf16_f32 v48, v182, v186
	v_cvt_pk_bf16_f32 v49, v190, v194
	global_store_dwordx4 v42, v[46:49], s[14:15] nt
	v_cvt_pk_bf16_f32 v50, v167, v171
	v_cvt_pk_bf16_f32 v51, v175, v179
	v_cvt_pk_bf16_f32 v52, v183, v187
	v_cvt_pk_bf16_f32 v53, v191, v195
	global_store_dwordx4 v43, v[50:53], s[14:15] nt
	v_cvt_pk_bf16_f32 v46, v168, v172
	v_cvt_pk_bf16_f32 v47, v176, v180
	v_cvt_pk_bf16_f32 v48, v184, v188
	v_cvt_pk_bf16_f32 v49, v192, v196
	global_store_dwordx4 v44, v[46:49], s[14:15] nt
	v_cvt_pk_bf16_f32 v50, v169, v173
	v_cvt_pk_bf16_f32 v51, v177, v181
	v_cvt_pk_bf16_f32 v52, v185, v189
	v_cvt_pk_bf16_f32 v53, v193, v197
	global_store_dwordx4 v45, v[50:53], s[14:15] nt
	global_load_dwordx4 v[166:169], v34, s[8:9] offset:896 nt
	global_load_dwordx4 v[170:173], v35, s[8:9] offset:896 nt
	global_load_dwordx4 v[174:177], v36, s[8:9] offset:896 nt
	global_load_dwordx4 v[178:181], v37, s[8:9] offset:896 nt
	global_load_dwordx4 v[182:185], v38, s[8:9] offset:896 nt
	global_load_dwordx4 v[186:189], v39, s[8:9] offset:896 nt
	global_load_dwordx4 v[190:193], v40, s[8:9] offset:896 nt
	global_load_dwordx4 v[194:197], v41, s[8:9] offset:896 nt
	s_waitcnt vmcnt(36)
; #define GAS __attribute__((address_space(1)))
; #define LAS __attribute__((address_space(3)))
; #define LDS_WAIT() asm volatile("s_waitcnt lgkmcnt(0)" ::: "memory")
; __device__ __forceinline__ unsigned pk2(float lo, float hi) { unsigned r; asm("v_cvt_pk_bf16_f32 %0, %1, %2" : "=v"(r) : "v"(lo), "v"(hi)); return r; }
; __device__ __forceinline__ void t_store(const TItem& d, const f32x4 (&r)[8], LAS float* scr, int lane) {
; #pragma unroll
;     for (int i = 0; i < 8; ++i) *(LAS f32x4*)(scr + (8 * i + (lane >> 3)) * 32 + (((lane & 7) * 4 + 8 * i) & 31)) = r[i];
;     LDS_WAIT(); asm volatile("" ::: "memory");
;     const int c = lane >> 3, nl = lane & 7;
; #pragma unroll
;     for (int j = 0; j < 4; ++j) { const int n = nl + 8 * j; const LAS float* s = scr + (8 * c) * 32 + ((n + 8 * c) & 31);
;         v4u o; o.x = pk2(s[0 * 32], s[1 * 32]); o.y = pk2(s[2 * 32], s[3 * 32]); o.z = pk2(s[4 * 32], s[5 * 32]); o.w = pk2(s[6 * 32], s[7 * 32]);
;         __builtin_nontemporal_store(o, (GAS v4u*)(d.WT + (size_t)t_drow(d.kind, d.n0 + n) * d.K + d.k0 + 8 * c)); }
; __global__ void __launch_bounds__(512, 2) mk_fwd(Params p_unused) {
;     ...
;             for (unsigned tb = grab(); tb < NTICK; tb = grab()) {
;                 TItem a0 = decode((int)(2u * tb)); TItem a1 = a0; a1.n0 += 32;
;                 f32x4 ra[8], rb[8], rc[8], rd[8]; t_load(a0, ra, lane); t_load(a1, rb, lane);
;                 _Pragma("unroll 1") for (unsigned u = 0; u < 8u; u += 2u) {
;                     const TItem b0 = decode((int)(2u * (tb + u + 1u))); TItem b1 = b0; b1.n0 += 32;
;                     t_load(b0, rc, lane); t_load(b1, rd, lane);
;                     t_store(a0, ra, scr, lane); t_store(a1, rb, scr, lane);
;                     if (u + 2u < 8u) { a0 = decode((int)(2u * (tb + u + 2u))); a1 = a0; a1.n0 += 32; t_load(a0, ra, lane); t_load(a1, rb, lane); }
;                     t_store(b0, rc, scr, lane); t_store(b1, rd, scr, lane);
;                 }
	s_cmp_eq_u32 s25, 0
	s_movk_i32 s6, 0x80
	s_cmovk_i32 s6, 0x100
	s_add_u32 s6, s6, s24
	s_lshl_b32 s6, s6, s26
	s_add_u32 s14, s12, s6
	s_addc_u32 s15, s13, 0
	v_cvt_pk_bf16_f32 v46, v54, v58
	v_cvt_pk_bf16_f32 v47, v62, v66
	v_cvt_pk_bf16_f32 v48, v70, v74
	v_cvt_pk_bf16_f32 v49, v78, v82
	global_store_dwordx4 v42, v[46:49], s[14:15] nt
	v_cvt_pk_bf16_f32 v50, v55, v59
	v_cvt_pk_bf16_f32 v51, v63, v67
	v_cvt_pk_bf16_f32 v52, v71, v75
	v_cvt_pk_bf16_f32 v53, v79, v83
	global_store_dwordx4 v43, v[50:53], s[14:15] nt
	v_cvt_pk_bf16_f32 v46, v56, v60
	v_cvt_pk_bf16_f32 v47, v64, v68
	v_cvt_pk_bf16_f32 v48, v72, v76
	v_cvt_pk_bf16_f32 v49, v80, v84
	global_store_dwordx4 v44, v[46:49], s[14:15] nt
	v_cvt_pk_bf16_f32 v50, v57, v61
	v_cvt_pk_bf16_f32 v51, v65, v69
	v_cvt_pk_bf16_f32 v52, v73, v77
	v_cvt_pk_bf16_f32 v53, v81, v85
	global_store_dwordx4 v45, v[50:53], s[14:15] nt
	global_load_dwordx4 v[54:57], v34, s[8:9] offset:1024 nt
	global_load_dwordx4 v[58:61], v35, s[8:9] offset:1024 nt
	global_load_dwordx4 v[62:65], v36, s[8:9] offset:1024 nt
	global_load_dwordx4 v[66:69], v37, s[8:9] offset:1024 nt
	global_load_dwordx4 v[70:73], v38, s[8:9] offset:1024 nt
	global_load_dwordx4 v[74:77], v39, s[8:9] offset:1024 nt
	global_load_dwordx4 v[78:81], v40, s[8:9] offset:1024 nt
	global_load_dwordx4 v[82:85], v41, s[8:9] offset:1024 nt
	s_waitcnt vmcnt(36)
	s_cmp_eq_u32 s25, 0
	s_movk_i32 s6, 0xa0
	s_cmovk_i32 s6, 0x120
	s_add_u32 s6, s6, s24
	s_lshl_b32 s6, s6, s26
	s_add_u32 s14, s12, s6
	s_addc_u32 s15, s13, 0
	v_cvt_pk_bf16_f32 v46, v86, v90
	v_cvt_pk_bf16_f32 v47, v94, v98
	v_cvt_pk_bf16_f32 v48, v102, v106
	v_cvt_pk_bf16_f32 v49, v110, v114
	global_store_dwordx4 v42, v[46:49], s[14:15] nt
	v_cvt_pk_bf16_f32 v50, v87, v91
	v_cvt_pk_bf16_f32 v51, v95, v99
	v_cvt_pk_bf16_f32 v52, v103, v107
	v_cvt_pk_bf16_f32 v53, v111, v115
	global_store_dwordx4 v43, v[50:53], s[14:15] nt
	v_cvt_pk_bf16_f32 v46, v88, v92
	v_cvt_pk_bf16_f32 v47, v96, v100
	v_cvt_pk_bf16_f32 v48, v104, v108
	v_cvt_pk_bf16_f32 v49, v112, v116
	global_store_dwordx4 v44, v[46:49], s[14:15] nt
	v_cvt_pk_bf16_f32 v50, v89, v93
	v_cvt_pk_bf16_f32 v51, v97, v101
	v_cvt_pk_bf16_f32 v52, v105, v109
	v_cvt_pk_bf16_f32 v53, v113, v117
	global_store_dwordx4 v45, v[50:53], s[14:15] nt
	global_load_dwordx4 v[86:89], v34, s[8:9] offset:1152 nt
	global_load_dwordx4 v[90:93], v35, s[8:9] offset:1152 nt
	global_load_dwordx4 v[94:97], v36, s[8:9] offset:1152 nt
	global_load_dwordx4 v[98:101], v37, s[8:9] offset:1152 nt
	global_load_dwordx4 v[102:105], v38, s[8:9] offset:1152 nt
	global_load_dwordx4 v[106:109], v39, s[8:9] offset:1152 nt
	global_load_dwordx4 v[110:113], v40, s[8:9] offset:1152 nt
	global_load_dwordx4 v[114:117], v41, s[8:9] offset:1152 nt
	s_waitcnt vmcnt(36)
	s_cmp_eq_u32 s25, 0
	s_movk_i32 s6, 0xc0
	s_cmovk_i32 s6, 0x140
	s_add_u32 s6, s6, s24
	s_lshl_b32 s6, s6, s26
	s_add_u32 s14, s12, s6
	s_addc_u32 s15, s13, 0
	v_cvt_pk_bf16_f32 v46, v118, v122
	v_cvt_pk_bf16_f32 v47, v126, v130
	v_cvt_pk_bf16_f32 v48, v134, v138
	v_cvt_pk_bf16_f32 v49, v142, v146
	global_store_dwordx4 v42, v[46:49], s[14:15] nt
	v_cvt_pk_bf16_f32 v50, v119, v123
	v_cvt_pk_bf16_f32 v51, v127, v131
	v_cvt_pk_bf16_f32 v52, v135, v139
	v_cvt_pk_bf16_f32 v53, v143, v147
	global_store_dwordx4 v43, v[50:53], s[14:15] nt
	v_cvt_pk_bf16_f32 v46, v120, v124
	v_cvt_pk_bf16_f32 v47, v128, v132
	v_cvt_pk_bf16_f32 v48, v136, v140
	v_cvt_pk_bf16_f32 v49, v144, v148
	global_store_dwordx4 v44, v[46:49], s[14:15] nt
	v_cvt_pk_bf16_f32 v50, v121, v125
	v_cvt_pk_bf16_f32 v51, v129, v133
	v_cvt_pk_bf16_f32 v52, v137, v141
	v_cvt_pk_bf16_f32 v53, v145, v149
	global_store_dwordx4 v45, v[50:53], s[14:15] nt
	global_load_dwordx4 v[118:121], v34, s[8:9] offset:1280 nt
	global_load_dwordx4 v[122:125], v35, s[8:9] offset:1280 nt
	global_load_dwordx4 v[126:129], v36, s[8:9] offset:1280 nt
	global_load_dwordx4 v[130:133], v37, s[8:9] offset:1280 nt
	global_load_dwordx4 v[134:137], v38, s[8:9] offset:1280 nt
	global_load_dwordx4 v[138:141], v39, s[8:9] offset:1280 nt
	global_load_dwordx4 v[142:145], v40, s[8:9] offset:1280 nt
	global_load_dwordx4 v[146:149], v41, s[8:9] offset:1280 nt
	s_waitcnt vmcnt(36)
	s_cmp_eq_u32 s25, 0
	s_movk_i32 s6, 0xe0
	s_cmovk_i32 s6, 0x160
	s_add_u32 s6, s6, s24
	s_lshl_b32 s6, s6, s26
	s_add_u32 s14, s12, s6
	s_addc_u32 s15, s13, 0
	v_cvt_pk_bf16_f32 v46, v166, v170
	v_cvt_pk_bf16_f32 v47, v174, v178
	v_cvt_pk_bf16_f32 v48, v182, v186
	v_cvt_pk_bf16_f32 v49, v190, v194
	global_store_dwordx4 v42, v[46:49], s[14:15] nt
	v_cvt_pk_bf16_f32 v50, v167, v171
	v_cvt_pk_bf16_f32 v51, v175, v179
	v_cvt_pk_bf16_f32 v52, v183, v187
	v_cvt_pk_bf16_f32 v53, v191, v195
	global_store_dwordx4 v43, v[50:53], s[14:15] nt
	v_cvt_pk_bf16_f32 v46, v168, v172
	v_cvt_pk_bf16_f32 v47, v176, v180
	v_cvt_pk_bf16_f32 v48, v184, v188
	v_cvt_pk_bf16_f32 v49, v192, v196
	global_store_dwordx4 v44, v[46:49], s[14:15] nt
	v_cvt_pk_bf16_f32 v50, v169, v173
	v_cvt_pk_bf16_f32 v51, v177, v181
	v_cvt_pk_bf16_f32 v52, v185, v189
	v_cvt_pk_bf16_f32 v53, v193, v197
	global_store_dwordx4 v45, v[50:53], s[14:15] nt
	global_load_dwordx4 v[166:169], v34, s[8:9] offset:1408 nt
	global_load_dwordx4 v[170:173], v35, s[8:9] offset:1408 nt
	global_load_dwordx4 v[174:177], v36, s[8:9] offset:1408 nt
	global_load_dwordx4 v[178:181], v37, s[8:9] offset:1408 nt
	global_load_dwordx4 v[182:185], v38, s[8:9] offset:1408 nt
	global_load_dwordx4 v[186:189], v39, s[8:9] offset:1408 nt
	global_load_dwordx4 v[190:193], v40, s[8:9] offset:1408 nt
	global_load_dwordx4 v[194:197], v41, s[8:9] offset:1408 nt
	s_waitcnt vmcnt(36)
; #define GAS __attribute__((address_space(1)))
; #define LAS __attribute__((address_space(3)))
; #define LDS_WAIT() asm volatile("s_waitcnt lgkmcnt(0)" ::: "memory")
; __device__ __forceinline__ unsigned pk2(float lo, float hi) { unsigned r; asm("v_cvt_pk_bf16_f32 %0, %1, %2" : "=v"(r) : "v"(lo), "v"(hi)); return r; }
; __device__ __forceinline__ void t_store(const TItem& d, const f32x4 (&r)[8], LAS float* scr, int lane) {
; #pragma unroll
;     for (int i = 0; i < 8; ++i) *(LAS f32x4*)(scr + (8 * i + (lane >> 3)) * 32 + (((lane & 7) * 4 + 8 * i) & 31)) = r[i];
;     LDS_WAIT(); asm volatile("" ::: "memory");
;     const int c = lane >> 3, nl = lane & 7;
; #pragma unroll
;     for (int j = 0; j < 4; ++j) { const int n = nl + 8 * j; const LAS float* s = scr + (8 * c) * 32 + ((n + 8 * c) & 31);
;         v4u o; o.x = pk2(s[0 * 32], s[1 * 32]); o.y = pk2(s[2 * 32], s[3 * 32]); o.z = pk2(s[4 * 32], s[5 * 32]); o.w = pk2(s[6 * 32], s[7 * 32]);
;         __builtin_nontemporal_store(o, (GAS v4u*)(d.WT + (size_t)t_drow(d.kind, d.n0 + n) * d.K + d.k0 + 8 * c)); }
; __global__ void __launch_bounds__(512, 2) mk_fwd(Params p_unused) {
;     ...
;             for (unsigned tb = grab(); tb < NTICK; tb = grab()) {
;                 TItem a0 = decode((int)(2u * tb)); TItem a1 = a0; a1.n0 += 32;
;                 f32x4 ra[8], rb[8], rc[8], rd[8]; t_load(a0, ra, lane); t_load(a1, rb, lane);
;                 _Pragma("unroll 1") for (unsigned u = 0; u < 8u; u += 2u) {
;                     const TItem b0 = decode((int)(2u * (tb + u + 1u))); TItem b1 = b0; b1.n0 += 32;
;                     t_load(b0, rc, lane); t_load(b1, rd, lane);
;                     t_store(a0, ra, scr, lane); t_store(a1, rb, scr, lane);
;                     if (u + 2u < 8u) { a0 = decode((int)(2u * (tb + u + 2u))); a1 = a0; a1.n0 += 32; t_load(a0, ra, lane); t_load(a1, rb, lane); }
;                     t_store(b0, rc, scr, lane); t_store(b1, rd, scr, lane);
;                 }
	s_cmp_eq_u32 s25, 0
	s_movk_i32 s6, 0x100
	s_cmovk_i32 s6, 0x200
	s_add_u32 s6, s6, s24
	s_lshl_b32 s6, s6, s26
	s_add_u32 s14, s12, s6
	s_addc_u32 s15, s13, 0
	v_cvt_pk_bf16_f32 v46, v54, v58
	v_cvt_pk_bf16_f32 v47, v62, v66
	v_cvt_pk_bf16_f32 v48, v70, v74
	v_cvt_pk_bf16_f32 v49, v78, v82
	global_store_dwordx4 v42, v[46:49], s[14:15] nt
	v_cvt_pk_bf16_f32 v50, v55, v59
	v_cvt_pk_bf16_f32 v51, v63, v67
	v_cvt_pk_bf16_f32 v52, v71, v75
	v_cvt_pk_bf16_f32 v53, v79, v83
	global_store_dwordx4 v43, v[50:53], s[14:15] nt
	v_cvt_pk_bf16_f32 v46, v56, v60
	v_cvt_pk_bf16_f32 v47, v64, v68
	v_cvt_pk_bf16_f32 v48, v72, v76
	v_cvt_pk_bf16_f32 v49, v80, v84
	global_store_dwordx4 v44, v[46:49], s[14:15] nt
	v_cvt_pk_bf16_f32 v50, v57, v61
	v_cvt_pk_bf16_f32 v51, v65, v69
	v_cvt_pk_bf16_f32 v52, v73, v77
	v_cvt_pk_bf16_f32 v53, v81, v85
	global_store_dwordx4 v45, v[50:53], s[14:15] nt
	global_load_dwordx4 v[54:57], v34, s[8:9] offset:1536 nt
	global_load_dwordx4 v[58:61], v35, s[8:9] offset:1536 nt
	global_load_dwordx4 v[62:65], v36, s[8:9] offset:1536 nt
	global_load_dwordx4 v[66:69], v37, s[8:9] offset:1536 nt
	global_load_dwordx4 v[70:73], v38, s[8:9] offset:1536 nt
	global_load_dwordx4 v[74:77], v39, s[8:9] offset:1536 nt
	global_load_dwordx4 v[78:81], v40, s[8:9] offset:1536 nt
	global_load_dwordx4 v[82:85], v41, s[8:9] offset:1536 nt
	s_waitcnt vmcnt(36)
	s_cmp_eq_u32 s25, 0
	s_movk_i32 s6, 0x120
	s_cmovk_i32 s6, 0x220
	s_add_u32 s6, s6, s24
	s_lshl_b32 s6, s6, s26
	s_add_u32 s14, s12, s6
	s_addc_u32 s15, s13, 0
	v_cvt_pk_bf16_f32 v46, v86, v90
	v_cvt_pk_bf16_f32 v47, v94, v98
	v_cvt_pk_bf16_f32 v48, v102, v106
	v_cvt_pk_bf16_f32 v49, v110, v114
	global_store_dwordx4 v42, v[46:49], s[14:15] nt
	v_cvt_pk_bf16_f32 v50, v87, v91
	v_cvt_pk_bf16_f32 v51, v95, v99
	v_cvt_pk_bf16_f32 v52, v103, v107
	v_cvt_pk_bf16_f32 v53, v111, v115
	global_store_dwordx4 v43, v[50:53], s[14:15] nt
	v_cvt_pk_bf16_f32 v46, v88, v92
	v_cvt_pk_bf16_f32 v47, v96, v100
	v_cvt_pk_bf16_f32 v48, v104, v108
	v_cvt_pk_bf16_f32 v49, v112, v116
	global_store_dwordx4 v44, v[46:49], s[14:15] nt
	v_cvt_pk_bf16_f32 v50, v89, v93
	v_cvt_pk_bf16_f32 v51, v97, v101
	v_cvt_pk_bf16_f32 v52, v105, v109
	v_cvt_pk_bf16_f32 v53, v113, v117
	global_store_dwordx4 v45, v[50:53], s[14:15] nt
	global_load_dwordx4 v[86:89], v34, s[8:9] offset:1664 nt
	global_load_dwordx4 v[90:93], v35, s[8:9] offset:1664 nt
	global_load_dwordx4 v[94:97], v36, s[8:9] offset:1664 nt
	global_load_dwordx4 v[98:101], v37, s[8:9] offset:1664 nt
	global_load_dwordx4 v[102:105], v38, s[8:9] offset:1664 nt
	global_load_dwordx4 v[106:109], v39, s[8:9] offset:1664 nt
	global_load_dwordx4 v[110:113], v40, s[8:9] offset:1664 nt
	global_load_dwordx4 v[114:117], v41, s[8:9] offset:1664 nt
	s_waitcnt vmcnt(36)
	s_cmp_eq_u32 s25, 0
	s_movk_i32 s6, 0x140
	s_cmovk_i32 s6, 0x240
	s_add_u32 s6, s6, s24
	s_lshl_b32 s6, s6, s26
	s_add_u32 s14, s12, s6
	s_addc_u32 s15, s13, 0
	v_cvt_pk_bf16_f32 v46, v118, v122
	v_cvt_pk_bf16_f32 v47, v126, v130
	v_cvt_pk_bf16_f32 v48, v134, v138
	v_cvt_pk_bf16_f32 v49, v142, v146
	global_store_dwordx4 v42, v[46:49], s[14:15] nt
	v_cvt_pk_bf16_f32 v50, v119, v123
	v_cvt_pk_bf16_f32 v51, v127, v131
	v_cvt_pk_bf16_f32 v52, v135, v139
	v_cvt_pk_bf16_f32 v53, v143, v147
	global_store_dwordx4 v43, v[50:53], s[14:15] nt
	v_cvt_pk_bf16_f32 v46, v120, v124
	v_cvt_pk_bf16_f32 v47, v128, v132
	v_cvt_pk_bf16_f32 v48, v136, v140
	v_cvt_pk_bf16_f32 v49, v144, v148
	global_store_dwordx4 v44, v[46:49], s[14:15] nt
	v_cvt_pk_bf16_f32 v50, v121, v125
	v_cvt_pk_bf16_f32 v51, v129, v133
	v_cvt_pk_bf16_f32 v52, v137, v141
	v_cvt_pk_bf16_f32 v53, v145, v149
	global_store_dwordx4 v45, v[50:53], s[14:15] nt
	global_load_dwordx4 v[118:121], v34, s[8:9] offset:1792 nt
	global_load_dwordx4 v[122:125], v35, s[8:9] offset:1792 nt
	global_load_dwordx4 v[126:129], v36, s[8:9] offset:1792 nt
	global_load_dwordx4 v[130:133], v37, s[8:9] offset:1792 nt
	global_load_dwordx4 v[134:137], v38, s[8:9] offset:1792 nt
	global_load_dwordx4 v[138:141], v39, s[8:9] offset:1792 nt
	global_load_dwordx4 v[142:145], v40, s[8:9] offset:1792 nt
	global_load_dwordx4 v[146:149], v41, s[8:9] offset:1792 nt
	s_waitcnt vmcnt(36)
	s_cmp_eq_u32 s25, 0
	s_movk_i32 s6, 0x160
	s_cmovk_i32 s6, 0x260
	s_add_u32 s6, s6, s24
	s_lshl_b32 s6, s6, s26
	s_add_u32 s14, s12, s6
	s_addc_u32 s15, s13, 0
	v_cvt_pk_bf16_f32 v46, v166, v170
	v_cvt_pk_bf16_f32 v47, v174, v178
	v_cvt_pk_bf16_f32 v48, v182, v186
	v_cvt_pk_bf16_f32 v49, v190, v194
	global_store_dwordx4 v42, v[46:49], s[14:15] nt
	v_cvt_pk_bf16_f32 v50, v167, v171
	v_cvt_pk_bf16_f32 v51, v175, v179
	v_cvt_pk_bf16_f32 v52, v183, v187
	v_cvt_pk_bf16_f32 v53, v191, v195
	global_store_dwordx4 v43, v[50:53], s[14:15] nt
	v_cvt_pk_bf16_f32 v46, v168, v172
	v_cvt_pk_bf16_f32 v47, v176, v180
	v_cvt_pk_bf16_f32 v48, v184, v188
	v_cvt_pk_bf16_f32 v49, v192, v196
	global_store_dwordx4 v44, v[46:49], s[14:15] nt
	v_cvt_pk_bf16_f32 v50, v169, v173
	v_cvt_pk_bf16_f32 v51, v177, v181
	v_cvt_pk_bf16_f32 v52, v185, v189
	v_cvt_pk_bf16_f32 v53, v193, v197
	global_store_dwordx4 v45, v[50:53], s[14:15] nt
	global_load_dwordx4 v[166:169], v34, s[8:9] offset:1920 nt
	global_load_dwordx4 v[170:173], v35, s[8:9] offset:1920 nt
	global_load_dwordx4 v[174:177], v36, s[8:9] offset:1920 nt
	global_load_dwordx4 v[178:181], v37, s[8:9] offset:1920 nt
	global_load_dwordx4 v[182:185], v38, s[8:9] offset:1920 nt
	global_load_dwordx4 v[186:189], v39, s[8:9] offset:1920 nt
	global_load_dwordx4 v[190:193], v40, s[8:9] offset:1920 nt
	global_load_dwordx4 v[194:197], v41, s[8:9] offset:1920 nt
	s_waitcnt vmcnt(36)
; __device__ __forceinline__ int obid() { int t = blockIdx.x; asm volatile("" : "+s"(t)); return t; }
; __global__ void __launch_bounds__(512, 2) mk_fwd(Params p_unused) {
;     ...
;             for (unsigned tb = grab(); tb < NTICK; tb = grab()) {
;                 TItem a0 = decode((int)(2u * tb)); TItem a1 = a0; a1.n0 += 32;
;                 f32x4 ra[8], rb[8], rc[8], rd[8]; t_load(a0, ra, lane); t_load(a1, rb, lane);
;                 _Pragma("unroll 1") for (unsigned u = 0; u < 8u; u += 2u) {
;                     const TItem b0 = decode((int)(2u * (tb + u + 1u))); TItem b1 = b0; b1.n0 += 32;
;                     t_load(b0, rc, lane); t_load(b1, rd, lane);
;                     t_store(a0, ra, scr, lane); t_store(a1, rb, scr, lane);
;                     if (u + 2u < 8u) { a0 = decode((int)(2u * (tb + u + 2u))); a1 = a0; a1.n0 += 32; t_load(a0, ra, lane); t_load(a1, rb, lane); }
;                     t_store(b0, rc, scr, lane); t_store(b1, rd, scr, lane);
;                 }
;             }
;         }
;         __syncthreads();
;         {
;             unsigned* wq = WSP(unsigned, WS_CTL) + CW_WQ; unsigned* done = WSP(unsigned, WS_CTL) + CW_DONE; unsigned* yd = WSP(unsigned, WS_CTL) + CW_YD; unsigned* bw = WSP(unsigned, WS_CTL) + CW_BAR;
;             const char* Oc = WSP(const char, WS_O); const char* Wc = WSP(const char, WS_WO);
;             pg8::Gemm g{DM, DM, DM}; pg8::EpiBf16W E{WSP(bf16_t, WS_Y), DM};
;             int tail = obid(); bool queue = true;
	s_cmp_eq_u32 s25, 0
	s_movk_i32 s6, 0x180
	s_cmovk_i32 s6, 0x300
	s_add_u32 s6, s6, s24
	s_lshl_b32 s6, s6, s26
	s_add_u32 s14, s12, s6
	s_addc_u32 s15, s13, 0
	v_cvt_pk_bf16_f32 v46, v54, v58
	v_cvt_pk_bf16_f32 v47, v62, v66
	v_cvt_pk_bf16_f32 v48, v70, v74
	v_cvt_pk_bf16_f32 v49, v78, v82
	global_store_dwordx4 v42, v[46:49], s[14:15] nt
	v_cvt_pk_bf16_f32 v50, v55, v59
	v_cvt_pk_bf16_f32 v51, v63, v67
	v_cvt_pk_bf16_f32 v52, v71, v75
	v_cvt_pk_bf16_f32 v53, v79, v83
	global_store_dwordx4 v43, v[50:53], s[14:15] nt
	v_cvt_pk_bf16_f32 v46, v56, v60
	v_cvt_pk_bf16_f32 v47, v64, v68
	v_cvt_pk_bf16_f32 v48, v72, v76
	v_cvt_pk_bf16_f32 v49, v80, v84
	global_store_dwordx4 v44, v[46:49], s[14:15] nt
	v_cvt_pk_bf16_f32 v50, v57, v61
	v_cvt_pk_bf16_f32 v51, v65, v69
	v_cvt_pk_bf16_f32 v52, v73, v77
	v_cvt_pk_bf16_f32 v53, v81, v85
	global_store_dwordx4 v45, v[50:53], s[14:15] nt
	s_waitcnt vmcnt(28)
	s_cmp_eq_u32 s25, 0
	s_movk_i32 s6, 0x1a0
	s_cmovk_i32 s6, 0x320
	s_add_u32 s6, s6, s24
	s_lshl_b32 s6, s6, s26
	s_add_u32 s14, s12, s6
	s_addc_u32 s15, s13, 0
	v_cvt_pk_bf16_f32 v46, v86, v90
	v_cvt_pk_bf16_f32 v47, v94, v98
	v_cvt_pk_bf16_f32 v48, v102, v106
	v_cvt_pk_bf16_f32 v49, v110, v114
	global_store_dwordx4 v42, v[46:49], s[14:15] nt
	v_cvt_pk_bf16_f32 v50, v87, v91
	v_cvt_pk_bf16_f32 v51, v95, v99
	v_cvt_pk_bf16_f32 v52, v103, v107
	v_cvt_pk_bf16_f32 v53, v111, v115
	global_store_dwordx4 v43, v[50:53], s[14:15] nt
	v_cvt_pk_bf16_f32 v46, v88, v92
	v_cvt_pk_bf16_f32 v47, v96, v100
	v_cvt_pk_bf16_f32 v48, v104, v108
	v_cvt_pk_bf16_f32 v49, v112, v116
	global_store_dwordx4 v44, v[46:49], s[14:15] nt
	v_cvt_pk_bf16_f32 v50, v89, v93
	v_cvt_pk_bf16_f32 v51, v97, v101
	v_cvt_pk_bf16_f32 v52, v105, v109
	v_cvt_pk_bf16_f32 v53, v113, v117
	global_store_dwordx4 v45, v[50:53], s[14:15] nt
	s_waitcnt vmcnt(20)
	s_cmp_eq_u32 s25, 0
	s_movk_i32 s6, 0x1c0
	s_cmovk_i32 s6, 0x340
	s_add_u32 s6, s6, s24
	s_lshl_b32 s6, s6, s26
	s_add_u32 s14, s12, s6
	s_addc_u32 s15, s13, 0
	v_cvt_pk_bf16_f32 v46, v118, v122
	v_cvt_pk_bf16_f32 v47, v126, v130
	v_cvt_pk_bf16_f32 v48, v134, v138
	v_cvt_pk_bf16_f32 v49, v142, v146
	global_store_dwordx4 v42, v[46:49], s[14:15] nt
	v_cvt_pk_bf16_f32 v50, v119, v123
	v_cvt_pk_bf16_f32 v51, v127, v131
	v_cvt_pk_bf16_f32 v52, v135, v139
	v_cvt_pk_bf16_f32 v53, v143, v147
	global_store_dwordx4 v43, v[50:53], s[14:15] nt
	v_cvt_pk_bf16_f32 v46, v120, v124
	v_cvt_pk_bf16_f32 v47, v128, v132
	v_cvt_pk_bf16_f32 v48, v136, v140
	v_cvt_pk_bf16_f32 v49, v144, v148
	global_store_dwordx4 v44, v[46:49], s[14:15] nt
	v_cvt_pk_bf16_f32 v50, v121, v125
	v_cvt_pk_bf16_f32 v51, v129, v133
	v_cvt_pk_bf16_f32 v52, v137, v141
	v_cvt_pk_bf16_f32 v53, v145, v149
	global_store_dwordx4 v45, v[50:53], s[14:15] nt
	s_waitcnt vmcnt(12)
	s_cmp_eq_u32 s25, 0
	s_movk_i32 s6, 0x1e0
	s_cmovk_i32 s6, 0x360
	s_add_u32 s6, s6, s24
	s_lshl_b32 s6, s6, s26
	s_add_u32 s14, s12, s6
	s_addc_u32 s15, s13, 0
	v_cvt_pk_bf16_f32 v46, v166, v170
	v_cvt_pk_bf16_f32 v47, v174, v178
	v_cvt_pk_bf16_f32 v48, v182, v186
	v_cvt_pk_bf16_f32 v49, v190, v194
	global_store_dwordx4 v42, v[46:49], s[14:15] nt
	v_cvt_pk_bf16_f32 v50, v167, v171
	v_cvt_pk_bf16_f32 v51, v175, v179
	v_cvt_pk_bf16_f32 v52, v183, v187
	v_cvt_pk_bf16_f32 v53, v191, v195
	global_store_dwordx4 v43, v[50:53], s[14:15] nt
	v_cvt_pk_bf16_f32 v46, v168, v172
	v_cvt_pk_bf16_f32 v47, v176, v180
	v_cvt_pk_bf16_f32 v48, v184, v188
	v_cvt_pk_bf16_f32 v49, v192, v196
	global_store_dwordx4 v44, v[46:49], s[14:15] nt
	v_cvt_pk_bf16_f32 v50, v169, v173
	v_cvt_pk_bf16_f32 v51, v177, v181
	v_cvt_pk_bf16_f32 v52, v185, v189
	v_cvt_pk_bf16_f32 v53, v193, v197
	global_store_dwordx4 v45, v[50:53], s[14:15] nt
	v_readfirstlane_b32 s40, v7
	s_nop 3
	s_branch .Lcv_loop
.Lcv_done:
	s_waitcnt vmcnt(0)
.LBB0_509:
	s_add_u32 s2, s28, 0x3080
	s_addc_u32 s3, s29, 0
	s_add_u32 s4, s28, 0x8000
	s_addc_u32 s5, s29, 0
	s_add_u32 s60, s28, 0x28000
	s_addc_u32 s61, s29, 0
	s_add_u32 s62, s28, 0xe00000
	s_addc_u32 s63, s29, 0
	s_add_u32 s6, s28, 0x31800000
	s_addc_u32 s7, s29, 0
	s_add_u32 s8, s28, 0x4200
	s_addc_u32 s9, s29, 0
	s_add_i32 s67, 0, 0x20080
	s_add_i32 s68, 0, 0x20084
	s_mov_b32 s64, s96
	s_mov_b64 s[40:41], -1
	s_mov_b32 s11, 0
	v_mov_b32_e32 v131, 0
	s_movk_i32 s65, 0x19f
	s_movk_i32 s66, 0x1b0
	s_mov_b32 s69, 0xfffe0
	s_mov_b32 s70, 0x80000
	s_mov_b64 s[12:13], 0x80000
	s_mov_b64 s[14:15], 0x80
	s_mov_b64 s[16:17], 0x100
	s_mov_b64 s[18:19], 0x80100
	s_mov_b64 s[20:21], 0x90000
	s_mov_b64 s[24:25], 0x90100
	s_mov_b64 s[26:27], 0xa0000
	s_mov_b64 s[30:31], 0xa0100
	s_mov_b64 s[34:35], 0xb0000
	s_mov_b64 s[36:37], 0xb0100
	v_mov_b32_e32 v1, s67
	v_mov_b32_e32 v146, s68
	v_mov_b32_e32 v147, 1
	s_barrier
	s_branch .LBB0_511
